# HGRN chunk-local loop: units after the first wait at the loop head only until 12 VMEM ops remain (vmcnt(12)) instead of the compiler's ladder down to 0
# baseline (speedup 1.0000x reference)
.LBB0_181:
	s_cmp_lg_u32 s56, s64
	s_cbranch_scc1 .Lhl_later
	s_waitcnt vmcnt(0)
	s_branch .Lhl_go
.Lhl_later:
	s_waitcnt vmcnt(12)
